# v99 + softmax exp runs prioritised in the attention tile loops (s_setprio 1 around each run of 15-16 v_exp, 32 runs)
# baseline (speedup 1.0000x reference)
.LBB0_499:
	s_waitcnt lgkmcnt(7)
	v_mfma_f32_32x32x16_bf16 v[82:97], v[80:83], v[162:165], 0
	s_waitcnt lgkmcnt(6)
	v_mfma_f32_32x32x16_bf16 v[98:113], v[98:101], v[162:165], 0
	s_waitcnt lgkmcnt(5)
	v_mfma_f32_32x32x16_bf16 v[82:97], v[132:135], v[166:169], v[82:97]
	s_waitcnt lgkmcnt(4)
	v_mfma_f32_32x32x16_bf16 v[98:113], v[76:79], v[166:169], v[98:113]
	s_waitcnt lgkmcnt(3)
	v_mfma_f32_32x32x16_bf16 v[82:97], v[128:131], v[170:173], v[82:97]
	s_waitcnt lgkmcnt(2)
	v_mfma_f32_32x32x16_bf16 v[98:113], v[68:71], v[170:173], v[98:113]
	s_waitcnt lgkmcnt(1)
	v_mfma_f32_32x32x16_bf16 v[82:97], v[72:75], v[174:177], v[82:97]
	s_waitcnt lgkmcnt(0)
	v_mfma_f32_32x32x16_bf16 v[98:113], v[64:67], v[174:177], v[98:113]
	s_barrier
	v_cndmask_b32_e64 v64, 0, 1, s[40:41]
	v_cmp_ne_u32_e64 s[42:43], 1, v64
	s_andn2_b64 vcc, exec, s[40:41]
	s_mov_b64 s[2:3], -1
	s_cbranch_vccnz .LBB0_503
	s_nop 3
	s_setprio 1
	v_exp_f32_e32 v64, v82
	v_exp_f32_e32 v65, v83
	v_exp_f32_e32 v66, v84
	v_exp_f32_e32 v67, v85
	v_exp_f32_e32 v68, v86
	v_exp_f32_e32 v69, v87
	v_exp_f32_e32 v70, v88
	v_exp_f32_e32 v71, v89
	v_exp_f32_e32 v72, v90
	v_exp_f32_e32 v73, v91
	v_exp_f32_e32 v74, v92
	v_exp_f32_e32 v75, v93
	v_exp_f32_e32 v76, v94
	v_exp_f32_e32 v77, v95
	v_exp_f32_e32 v78, v96
	s_setprio 0
	s_cbranch_execz .LBB0_504

.LBB0_502:
	s_nop 0
	s_setprio 1
	v_exp_f32_e32 v80, v98
	v_exp_f32_e32 v81, v99
	v_exp_f32_e32 v82, v100
	v_exp_f32_e32 v83, v101
	v_exp_f32_e32 v84, v102
	v_exp_f32_e32 v85, v103
	v_exp_f32_e32 v86, v104
	v_exp_f32_e32 v87, v105
	v_exp_f32_e32 v88, v106
	v_exp_f32_e32 v89, v107
	v_exp_f32_e32 v90, v108
	v_exp_f32_e32 v91, v109
	v_exp_f32_e32 v92, v110
	v_exp_f32_e32 v93, v111
	v_exp_f32_e32 v94, v112
	s_setprio 0
	s_cbranch_execz .LBB0_506

.LBB0_509:
	ds_read_b128 v[112:115], v142 offset:49152
	ds_read_b128 v[128:131], v142 offset:57344
	ds_read_b128 v[146:149], v143 offset:49152
	ds_read_b128 v[150:153], v143 offset:57344
	ds_read_b128 v[154:157], v144 offset:49152
	ds_read_b128 v[218:221], v144 offset:57344
	ds_read_b128 v[222:225], v145 offset:49152
	ds_read_b128 v[226:229], v145 offset:57344
	ds_read_b64_tr_b16 v[116:117], v212 offset:0
	ds_read_b64_tr_b16 v[118:119], v212 offset:0x800
	ds_read_b64_tr_b16 v[120:121], v212 offset:0x1000
	ds_read_b64_tr_b16 v[122:123], v212 offset:0x1800
	ds_read_b64_tr_b16 v[124:125], v212 offset:0x2000
	ds_read_b64_tr_b16 v[126:127], v212 offset:0x2800
	ds_read_b64_tr_b16 v[132:133], v212 offset:0x3000
	ds_read_b64_tr_b16 v[134:135], v212 offset:0x3800
	s_waitcnt lgkmcnt(0)
	s_nop 0
	v_mfma_f32_32x32x16_bf16 v[0:15], v[96:99], v[116:119], v[0:15]
	ds_read_b64_tr_b16 v[116:117], v212 offset:0x200
	ds_read_b64_tr_b16 v[118:119], v212 offset:0xa00
	v_mfma_f32_32x32x16_bf16 v[0:15], v[100:103], v[120:123], v[0:15]
	ds_read_b64_tr_b16 v[120:121], v212 offset:0x1200
	ds_read_b64_tr_b16 v[122:123], v212 offset:0x1a00
	v_mfma_f32_32x32x16_bf16 v[0:15], v[104:107], v[124:127], v[0:15]
	ds_read_b64_tr_b16 v[124:125], v212 offset:0x2200
	ds_read_b64_tr_b16 v[126:127], v212 offset:0x2a00
	v_mfma_f32_32x32x16_bf16 v[0:15], v[108:111], v[132:135], v[0:15]
	ds_read_b64_tr_b16 v[132:133], v212 offset:0x3200
	ds_read_b64_tr_b16 v[134:135], v212 offset:0x3a00
	s_waitcnt lgkmcnt(0)
	v_mfma_f32_32x32x16_bf16 v[16:31], v[96:99], v[116:119], v[16:31]
	ds_read_b64_tr_b16 v[116:117], v212 offset:0x400
	ds_read_b64_tr_b16 v[118:119], v212 offset:0xc00
	v_mfma_f32_32x32x16_bf16 v[16:31], v[100:103], v[120:123], v[16:31]
	ds_read_b64_tr_b16 v[120:121], v212 offset:0x1400
	ds_read_b64_tr_b16 v[122:123], v212 offset:0x1c00
	v_mfma_f32_32x32x16_bf16 v[16:31], v[104:107], v[124:127], v[16:31]
	ds_read_b64_tr_b16 v[124:125], v212 offset:0x2400
	ds_read_b64_tr_b16 v[126:127], v212 offset:0x2c00
	v_mfma_f32_32x32x16_bf16 v[16:31], v[108:111], v[132:135], v[16:31]
	ds_read_b64_tr_b16 v[132:133], v212 offset:0x3400
	ds_read_b64_tr_b16 v[134:135], v212 offset:0x3c00
	s_waitcnt lgkmcnt(0)
	v_mfma_f32_32x32x16_bf16 v[32:47], v[96:99], v[116:119], v[32:47]
	ds_read_b64_tr_b16 v[116:117], v212 offset:0x600
	ds_read_b64_tr_b16 v[118:119], v212 offset:0xe00
	v_mfma_f32_32x32x16_bf16 v[32:47], v[100:103], v[120:123], v[32:47]
	ds_read_b64_tr_b16 v[120:121], v212 offset:0x1600
	ds_read_b64_tr_b16 v[122:123], v212 offset:0x1e00
	v_mfma_f32_32x32x16_bf16 v[32:47], v[104:107], v[124:127], v[32:47]
	ds_read_b64_tr_b16 v[124:125], v212 offset:0x2600
	ds_read_b64_tr_b16 v[126:127], v212 offset:0x2e00
	v_mfma_f32_32x32x16_bf16 v[32:47], v[108:111], v[132:135], v[32:47]
	ds_read_b64_tr_b16 v[132:133], v212 offset:0x3600
	ds_read_b64_tr_b16 v[134:135], v212 offset:0x3e00
	s_waitcnt lgkmcnt(0)
	v_mfma_f32_32x32x16_bf16 v[48:63], v[96:99], v[116:119], v[48:63]
	v_mfma_f32_32x32x16_bf16 v[48:63], v[100:103], v[120:123], v[48:63]
	v_mfma_f32_32x32x16_bf16 v[48:63], v[104:107], v[124:127], v[48:63]
	v_mfma_f32_32x32x16_bf16 v[48:63], v[108:111], v[132:135], v[48:63]
	s_waitcnt lgkmcnt(7)
	v_mfma_f32_32x32x16_bf16 v[112:127], v[112:115], v[162:165], 0
	s_waitcnt lgkmcnt(6)
	v_mfma_f32_32x32x16_bf16 v[128:143], v[128:131], v[162:165], 0
	s_waitcnt lgkmcnt(5)
	v_mfma_f32_32x32x16_bf16 v[112:127], v[146:149], v[166:169], v[112:127]
	s_waitcnt lgkmcnt(4)
	v_mfma_f32_32x32x16_bf16 v[128:143], v[150:153], v[166:169], v[128:143]
	s_waitcnt lgkmcnt(3)
	v_mfma_f32_32x32x16_bf16 v[112:127], v[154:157], v[170:173], v[112:127]
	s_waitcnt lgkmcnt(2)
	v_mfma_f32_32x32x16_bf16 v[128:143], v[218:221], v[170:173], v[128:143]
	s_waitcnt lgkmcnt(1)
	v_mfma_f32_32x32x16_bf16 v[112:127], v[222:225], v[174:177], v[112:127]
	s_waitcnt lgkmcnt(0)
	v_mfma_f32_32x32x16_bf16 v[128:143], v[226:229], v[174:177], v[128:143]
	s_barrier
	s_and_b64 vcc, exec, s[42:43]
	s_mov_b64 s[58:59], -1
	s_cbranch_vccnz .LBB0_513
	s_nop 5
	s_setprio 1
	v_exp_f32_e32 v96, v112
	v_exp_f32_e32 v97, v113
	v_exp_f32_e32 v98, v114
	v_exp_f32_e32 v99, v115
	v_exp_f32_e32 v100, v116
	v_exp_f32_e32 v101, v117
	v_exp_f32_e32 v102, v118
	v_exp_f32_e32 v103, v119
	v_exp_f32_e32 v104, v120
	v_exp_f32_e32 v105, v121
	v_exp_f32_e32 v106, v122
	v_exp_f32_e32 v107, v123
	v_exp_f32_e32 v108, v124
	v_exp_f32_e32 v109, v125
	v_exp_f32_e32 v110, v126
	s_setprio 0
	s_cbranch_execz .LBB0_514

.LBB0_512:
	s_nop 2
	s_setprio 1
	v_exp_f32_e32 v144, v128
	v_exp_f32_e32 v145, v129
	v_exp_f32_e32 v146, v130
	v_exp_f32_e32 v147, v131
	v_exp_f32_e32 v148, v132
	v_exp_f32_e32 v149, v133
	v_exp_f32_e32 v150, v134
	v_exp_f32_e32 v151, v135
	v_exp_f32_e32 v152, v136
	v_exp_f32_e32 v153, v137
	v_exp_f32_e32 v154, v138
	v_exp_f32_e32 v155, v139
	v_exp_f32_e32 v156, v140
	v_exp_f32_e32 v157, v141
	v_exp_f32_e32 v158, v142
	s_setprio 0
	s_cbranch_execz .LBB0_516

.LBB0_523:
	v_lshl_add_u64 v[132:133], s[74:75], 0, v[192:193]
	v_add_co_u32_e32 v64, vcc, s67, v132
	v_lshl_add_u64 v[130:131], s[74:75], 0, v[194:195]
	s_nop 0
	v_addc_co_u32_e32 v65, vcc, 0, v133, vcc
	v_add_co_u32_e32 v66, vcc, s67, v130
	v_lshl_add_u64 v[128:129], s[74:75], 0, v[160:161]
	s_nop 0
	v_addc_co_u32_e32 v67, vcc, 0, v131, vcc
	global_load_dwordx4 v[146:149], v[64:65], off offset:1024
	global_load_dwordx4 v[150:153], v[66:67], off offset:2048
	v_add_co_u32_e32 v64, vcc, s67, v128
	s_nop 1
	v_addc_co_u32_e32 v65, vcc, 0, v129, vcc
	global_load_dwordx4 v[154:157], v[64:65], off offset:2048
	v_add_u32_e32 v134, v206, v207
	v_add_u32_e32 v135, v206, v208
	v_add_u32_e32 v136, v206, v209
	v_add_u32_e32 v137, v206, v210
	ds_read_b128 v[64:67], v134 offset:32768
	ds_read_b128 v[68:71], v134 offset:40960
	ds_read_b128 v[72:75], v135 offset:32768
	ds_read_b128 v[76:79], v135 offset:40960
	ds_read_b128 v[80:83], v136 offset:32768
	ds_read_b128 v[84:87], v136 offset:40960
	ds_read_b128 v[88:91], v137 offset:32768
	ds_read_b128 v[92:95], v137 offset:40960
	s_waitcnt lgkmcnt(7)
	v_mfma_f32_32x32x16_bf16 v[112:127], v[64:67], v[162:165], 0
	s_waitcnt lgkmcnt(6)
	v_mfma_f32_32x32x16_bf16 v[96:111], v[68:71], v[162:165], 0
	s_waitcnt lgkmcnt(5)
	v_mfma_f32_32x32x16_bf16 v[112:127], v[72:75], v[166:169], v[112:127]
	s_waitcnt lgkmcnt(4)
	v_mfma_f32_32x32x16_bf16 v[96:111], v[76:79], v[166:169], v[96:111]
	s_waitcnt lgkmcnt(3)
	v_mfma_f32_32x32x16_bf16 v[112:127], v[80:83], v[170:173], v[112:127]
	s_waitcnt lgkmcnt(2)
	v_mfma_f32_32x32x16_bf16 v[96:111], v[84:87], v[170:173], v[96:111]
	s_waitcnt lgkmcnt(1)
	v_mfma_f32_32x32x16_bf16 v[112:127], v[88:91], v[174:177], v[112:127]
	s_waitcnt lgkmcnt(0)
	v_mfma_f32_32x32x16_bf16 v[96:111], v[92:95], v[174:177], v[96:111]
	v_cndmask_b32_e64 v64, 0, 1, s[40:41]
	v_cmp_ne_u32_e64 s[42:43], 1, v64
	s_andn2_b64 vcc, exec, s[40:41]
	s_mov_b64 s[2:3], -1
	s_cbranch_vccnz .LBB0_527
	s_nop 4
	s_setprio 1
	v_exp_f32_e32 v64, v112
	v_exp_f32_e32 v65, v113
	v_exp_f32_e32 v66, v114
	v_exp_f32_e32 v67, v115
	v_exp_f32_e32 v68, v116
	v_exp_f32_e32 v69, v117
	v_exp_f32_e32 v70, v118
	v_exp_f32_e32 v71, v119
	v_exp_f32_e32 v72, v120
	v_exp_f32_e32 v73, v121
	v_exp_f32_e32 v74, v122
	v_exp_f32_e32 v75, v123
	v_exp_f32_e32 v76, v124
	v_exp_f32_e32 v77, v125
	v_exp_f32_e32 v78, v126
	s_setprio 0
	s_cbranch_execz .LBB0_528

.LBB0_526:
	s_nop 1
	s_setprio 1
	v_exp_f32_e32 v80, v96
	v_exp_f32_e32 v81, v97
	v_exp_f32_e32 v82, v98
	v_exp_f32_e32 v83, v99
	v_exp_f32_e32 v84, v100
	v_exp_f32_e32 v85, v101
	v_exp_f32_e32 v86, v102
	v_exp_f32_e32 v87, v103
	v_exp_f32_e32 v88, v104
	v_exp_f32_e32 v89, v105
	v_exp_f32_e32 v90, v106
	v_exp_f32_e32 v91, v107
	v_exp_f32_e32 v92, v108
	v_exp_f32_e32 v93, v109
	v_exp_f32_e32 v94, v110
	s_setprio 0
	s_cbranch_execz .LBB0_530

.LBB0_533:
	ds_read_b128 v[96:99], v134 offset:49152
	ds_read_b128 v[100:103], v134 offset:57344
	ds_read_b128 v[104:107], v135 offset:49152
	ds_read_b128 v[108:111], v135 offset:57344
	ds_read_b128 v[178:181], v136 offset:49152
	ds_read_b128 v[182:185], v136 offset:57344
	ds_read_b128 v[186:189], v137 offset:49152
	ds_read_b128 v[196:199], v137 offset:57344
	s_waitcnt lgkmcnt(7)
	v_mfma_f32_32x32x16_bf16 v[114:129], v[96:99], v[162:165], 0
	s_waitcnt lgkmcnt(6)
	v_mfma_f32_32x32x16_bf16 v[130:145], v[100:103], v[162:165], 0
	s_waitcnt lgkmcnt(5)
	v_mfma_f32_32x32x16_bf16 v[114:129], v[104:107], v[166:169], v[114:129]
	s_waitcnt lgkmcnt(4)
	v_mfma_f32_32x32x16_bf16 v[130:145], v[108:111], v[166:169], v[130:145]
	s_waitcnt lgkmcnt(3)
	v_mfma_f32_32x32x16_bf16 v[114:129], v[178:181], v[170:173], v[114:129]
	s_waitcnt lgkmcnt(2)
	v_mfma_f32_32x32x16_bf16 v[130:145], v[182:185], v[170:173], v[130:145]
	s_waitcnt lgkmcnt(1)
	v_mfma_f32_32x32x16_bf16 v[114:129], v[186:189], v[174:177], v[114:129]
	s_waitcnt lgkmcnt(0)
	v_mfma_f32_32x32x16_bf16 v[130:145], v[196:199], v[174:177], v[130:145]
	s_and_b64 vcc, exec, s[42:43]
	s_mov_b64 s[58:59], -1
	s_cbranch_vccnz .LBB0_537
	s_nop 6
	s_setprio 1
	v_exp_f32_e32 v96, v114
	v_exp_f32_e32 v97, v115
	v_exp_f32_e32 v98, v116
	v_exp_f32_e32 v99, v117
	v_exp_f32_e32 v100, v118
	v_exp_f32_e32 v101, v119
	v_exp_f32_e32 v102, v120
	v_exp_f32_e32 v103, v121
	v_exp_f32_e32 v104, v122
	v_exp_f32_e32 v105, v123
	v_exp_f32_e32 v106, v124
	v_exp_f32_e32 v107, v125
	v_exp_f32_e32 v108, v126
	v_exp_f32_e32 v109, v127
	v_exp_f32_e32 v110, v128
	s_setprio 0
	s_cbranch_execz .LBB0_538

.LBB0_536:
	s_nop 3
	s_setprio 1
	v_exp_f32_e32 v112, v130
	v_exp_f32_e32 v113, v131
	v_exp_f32_e32 v114, v132
	v_exp_f32_e32 v115, v133
	v_exp_f32_e32 v116, v134
	v_exp_f32_e32 v117, v135
	v_exp_f32_e32 v118, v136
	v_exp_f32_e32 v119, v137
	v_exp_f32_e32 v120, v138
	v_exp_f32_e32 v121, v139
	v_exp_f32_e32 v122, v140
	v_exp_f32_e32 v123, v141
	v_exp_f32_e32 v124, v142
	v_exp_f32_e32 v125, v143
	v_exp_f32_e32 v126, v144
	s_setprio 0
	s_cbranch_execz .LBB0_540

.LBB0_574:
	v_lshl_add_u64 v[132:133], s[90:91], 0, v[192:193]
	v_add_co_u32_e32 v64, vcc, s67, v132
	v_lshl_add_u64 v[130:131], s[90:91], 0, v[194:195]
	s_nop 0
	v_addc_co_u32_e32 v65, vcc, 0, v133, vcc
	v_add_co_u32_e32 v66, vcc, s67, v130
	v_lshl_add_u64 v[128:129], s[90:91], 0, v[160:161]
	s_nop 0
	v_addc_co_u32_e32 v67, vcc, 0, v131, vcc
	global_load_dwordx4 v[146:149], v[64:65], off offset:1152
	global_load_dwordx4 v[150:153], v[66:67], off offset:2048
	v_add_co_u32_e32 v64, vcc, s67, v128
	s_nop 1
	v_addc_co_u32_e32 v65, vcc, 0, v129, vcc
	global_load_dwordx4 v[154:157], v[64:65], off offset:2048
	v_add_u32_e32 v134, v206, v207
	v_add_u32_e32 v135, v206, v208
	v_add_u32_e32 v136, v206, v209
	v_add_u32_e32 v137, v206, v210
	ds_read_b128 v[64:67], v134 offset:32768
	ds_read_b128 v[68:71], v134 offset:40960
	ds_read_b128 v[72:75], v135 offset:32768
	ds_read_b128 v[76:79], v135 offset:40960
	ds_read_b128 v[80:83], v136 offset:32768
	ds_read_b128 v[84:87], v136 offset:40960
	ds_read_b128 v[88:91], v137 offset:32768
	ds_read_b128 v[92:95], v137 offset:40960
	s_waitcnt lgkmcnt(7)
	v_mfma_f32_32x32x16_bf16 v[112:127], v[64:67], v[162:165], 0
	s_waitcnt lgkmcnt(6)
	v_mfma_f32_32x32x16_bf16 v[96:111], v[68:71], v[162:165], 0
	s_waitcnt lgkmcnt(5)
	v_mfma_f32_32x32x16_bf16 v[112:127], v[72:75], v[166:169], v[112:127]
	s_waitcnt lgkmcnt(4)
	v_mfma_f32_32x32x16_bf16 v[96:111], v[76:79], v[166:169], v[96:111]
	s_waitcnt lgkmcnt(3)
	v_mfma_f32_32x32x16_bf16 v[112:127], v[80:83], v[170:173], v[112:127]
	s_waitcnt lgkmcnt(2)
	v_mfma_f32_32x32x16_bf16 v[96:111], v[84:87], v[170:173], v[96:111]
	s_waitcnt lgkmcnt(1)
	v_mfma_f32_32x32x16_bf16 v[112:127], v[88:91], v[174:177], v[112:127]
	s_waitcnt lgkmcnt(0)
	v_mfma_f32_32x32x16_bf16 v[96:111], v[92:95], v[174:177], v[96:111]
	v_cndmask_b32_e64 v64, 0, 1, s[40:41]
	v_cmp_ne_u32_e64 s[42:43], 1, v64
	s_andn2_b64 vcc, exec, s[40:41]
	s_mov_b64 s[2:3], -1
	s_cbranch_vccnz .LBB0_578
	s_nop 4
	s_setprio 1
	v_exp_f32_e32 v64, v112
	v_exp_f32_e32 v65, v113
	v_exp_f32_e32 v66, v114
	v_exp_f32_e32 v67, v115
	v_exp_f32_e32 v68, v116
	v_exp_f32_e32 v69, v117
	v_exp_f32_e32 v70, v118
	v_exp_f32_e32 v71, v119
	v_exp_f32_e32 v72, v120
	v_exp_f32_e32 v73, v121
	v_exp_f32_e32 v74, v122
	v_exp_f32_e32 v75, v123
	v_exp_f32_e32 v76, v124
	v_exp_f32_e32 v77, v125
	v_exp_f32_e32 v78, v126
	s_setprio 0
	s_cbranch_execz .LBB0_579

.LBB0_606:
	v_lshl_add_u32 v64, v246, 8, 0
	v_add_u32_e32 v112, s44, v64
	v_add_u32_e32 v68, v112, v226
	v_add_u32_e32 v72, v112, v227
	ds_read_b128 v[64:67], v68 offset:32768
	ds_read_b128 v[68:71], v68 offset:40960
	ds_read_b128 v[96:99], v72 offset:32768
	ds_read_b128 v[100:103], v72 offset:40960
	s_waitcnt lgkmcnt(0)
	v_mfma_f32_32x32x16_bf16 v[114:129], v[64:67], v[162:165], 0
	v_mfma_f32_32x32x16_bf16 v[80:95], v[64:67], v[186:189], 0
	v_mfma_f32_32x32x16_bf16 v[130:145], v[68:71], v[162:165], 0
	v_mfma_f32_32x32x16_bf16 v[64:79], v[68:71], v[186:189], 0
	v_mfma_f32_32x32x16_bf16 v[114:129], v[96:99], v[166:169], v[114:129]
	v_mfma_f32_32x32x16_bf16 v[80:95], v[96:99], v[190:193], v[80:95]
	v_mfma_f32_32x32x16_bf16 v[130:145], v[100:103], v[166:169], v[130:145]
	v_mfma_f32_32x32x16_bf16 v[64:79], v[100:103], v[190:193], v[64:79]
	v_add_u32_e32 v100, v112, v238
	v_add_u32_e32 v108, v112, v239
	ds_read_b128 v[96:99], v100 offset:32768
	ds_read_b128 v[100:103], v100 offset:40960
	ds_read_b128 v[104:107], v108 offset:32768
	ds_read_b128 v[108:111], v108 offset:40960
	s_waitcnt lgkmcnt(0)
	v_mfma_f32_32x32x16_bf16 v[114:129], v[96:99], v[170:173], v[114:129]
	v_mfma_f32_32x32x16_bf16 v[80:95], v[96:99], v[194:197], v[80:95]
	v_mfma_f32_32x32x16_bf16 v[130:145], v[100:103], v[170:173], v[130:145]
	v_mfma_f32_32x32x16_bf16 v[64:79], v[100:103], v[194:197], v[64:79]
	v_mfma_f32_32x32x16_bf16 v[114:129], v[104:107], v[174:177], v[114:129]
	v_mfma_f32_32x32x16_bf16 v[80:95], v[104:107], v[198:201], v[80:95]
	v_mfma_f32_32x32x16_bf16 v[130:145], v[108:111], v[174:177], v[130:145]
	v_mfma_f32_32x32x16_bf16 v[64:79], v[108:111], v[198:201], v[64:79]
	v_add_u32_e32 v100, v112, v247
	v_add_u32_e32 v108, v112, v249
	ds_read_b128 v[96:99], v100 offset:32768
	ds_read_b128 v[100:103], v100 offset:40960
	ds_read_b128 v[104:107], v108 offset:32768
	ds_read_b128 v[108:111], v108 offset:40960
	s_waitcnt lgkmcnt(0)
	v_mfma_f32_32x32x16_bf16 v[114:129], v[96:99], v[178:181], v[114:129]
	v_mfma_f32_32x32x16_bf16 v[80:95], v[96:99], v[202:205], v[80:95]
	v_mfma_f32_32x32x16_bf16 v[130:145], v[100:103], v[178:181], v[130:145]
	v_mfma_f32_32x32x16_bf16 v[64:79], v[100:103], v[202:205], v[64:79]
	v_mfma_f32_32x32x16_bf16 v[114:129], v[104:107], v[182:185], v[114:129]
	v_mfma_f32_32x32x16_bf16 v[80:95], v[104:107], v[206:209], v[80:95]
	v_mfma_f32_32x32x16_bf16 v[130:145], v[108:111], v[182:185], v[130:145]
	v_mfma_f32_32x32x16_bf16 v[64:79], v[108:111], v[206:209], v[64:79]
	v_cndmask_b32_e64 v96, 0, 1, s[40:41]
	v_cmp_ne_u32_e64 s[44:45], 1, v96
	s_andn2_b64 vcc, exec, s[40:41]
	s_mov_b64 s[2:3], -1
	s_cbranch_vccnz .LBB0_610
	s_nop 3
	s_setprio 1
	v_exp_f32_e32 v96, v114
	v_exp_f32_e32 v97, v115
	v_exp_f32_e32 v98, v116
	v_exp_f32_e32 v99, v117
	v_exp_f32_e32 v100, v118
	v_exp_f32_e32 v101, v119
	v_exp_f32_e32 v102, v120
	v_exp_f32_e32 v103, v121
	v_exp_f32_e32 v104, v122
	v_exp_f32_e32 v105, v123
	v_exp_f32_e32 v106, v124
	v_exp_f32_e32 v107, v125
	v_exp_f32_e32 v108, v126
	v_exp_f32_e32 v109, v127
	v_exp_f32_e32 v110, v128
	s_setprio 0
	s_cbranch_execz .LBB0_611

.LBB0_609:
	s_nop 0
	s_setprio 1
	v_exp_f32_e32 v112, v130
	v_exp_f32_e32 v113, v131
	v_exp_f32_e32 v114, v132
	v_exp_f32_e32 v115, v133
	v_exp_f32_e32 v116, v134
	v_exp_f32_e32 v117, v135
	v_exp_f32_e32 v118, v136
	v_exp_f32_e32 v119, v137
	v_exp_f32_e32 v120, v138
	v_exp_f32_e32 v121, v139
	v_exp_f32_e32 v122, v140
	v_exp_f32_e32 v123, v141
	v_exp_f32_e32 v124, v142
	v_exp_f32_e32 v125, v143
	v_exp_f32_e32 v126, v144
	s_setprio 0
	s_cbranch_execz .LBB0_613
.LBB0_614:
	v_exp_f32_e32 v111, v129
	v_exp_f32_e32 v127, v145
	v_cvt_pk_bf16_f32 v210, v96, v97
	v_cvt_pk_bf16_f32 v211, v98, v99
	v_cvt_pk_bf16_f32 v212, v100, v101
	v_cvt_pk_bf16_f32 v213, v102, v103
	v_cvt_pk_bf16_f32 v218, v104, v105
	v_cvt_pk_bf16_f32 v219, v106, v107
	v_cvt_pk_bf16_f32 v220, v108, v109
	v_cvt_pk_bf16_f32 v221, v110, v111
	v_cvt_pk_bf16_f32 v222, v112, v113
	v_cvt_pk_bf16_f32 v223, v114, v115
	v_cvt_pk_bf16_f32 v224, v116, v117
	v_cvt_pk_bf16_f32 v225, v118, v119
	v_cvt_pk_bf16_f32 v214, v120, v121
	v_cvt_pk_bf16_f32 v215, v122, v123
	v_cvt_pk_bf16_f32 v216, v124, v125
	v_cvt_pk_bf16_f32 v217, v126, v127
	v_permlane32_swap_b32_e32 v210, v212
	v_permlane32_swap_b32_e32 v211, v213
	v_permlane32_swap_b32_e32 v218, v220
	v_permlane32_swap_b32_e32 v219, v221
	v_permlane32_swap_b32_e32 v222, v224
	v_permlane32_swap_b32_e32 v223, v225
	v_permlane32_swap_b32_e32 v214, v216
	v_permlane32_swap_b32_e32 v215, v217
	s_and_b64 vcc, exec, s[44:45]
	s_mov_b64 s[2:3], -1
	s_cbranch_vccnz .LBB0_618
	s_setprio 1
	v_exp_f32_e32 v128, v80
	v_exp_f32_e32 v129, v81
	v_exp_f32_e32 v130, v82
	v_exp_f32_e32 v131, v83
	v_exp_f32_e32 v132, v84
	v_exp_f32_e32 v133, v85
	v_exp_f32_e32 v134, v86
	v_exp_f32_e32 v135, v87
	v_exp_f32_e32 v136, v88
	v_exp_f32_e32 v137, v89
	v_exp_f32_e32 v138, v90
	v_exp_f32_e32 v139, v91
	v_exp_f32_e32 v140, v92
	v_exp_f32_e32 v141, v93
	v_exp_f32_e32 v142, v94
	s_setprio 0
	s_cbranch_execz .LBB0_619

.LBB0_617:
	s_setprio 1
	v_exp_f32_e32 v144, v64
	v_exp_f32_e32 v145, v65
	v_exp_f32_e32 v146, v66
	v_exp_f32_e32 v147, v67
	v_exp_f32_e32 v148, v68
	v_exp_f32_e32 v149, v69
	v_exp_f32_e32 v150, v70
	v_exp_f32_e32 v151, v71
	v_exp_f32_e32 v152, v72
	v_exp_f32_e32 v153, v73
	v_exp_f32_e32 v154, v74
	v_exp_f32_e32 v155, v75
	v_exp_f32_e32 v156, v76
	v_exp_f32_e32 v157, v77
	v_exp_f32_e32 v158, v78
	s_setprio 0
	s_cbranch_execnz .LBB0_601
	s_branch .LBB0_621

.LBB0_636:
	v_add_u32_e32 v104, s44, v221
	v_add_u32_e32 v68, v104, v222
	v_add_u32_e32 v72, v104, v223
	ds_read_b128 v[64:67], v68 offset:32768
	ds_read_b128 v[68:71], v68 offset:40960
	ds_read_b128 v[96:99], v72 offset:32768
	ds_read_b128 v[100:103], v72 offset:40960
	s_waitcnt lgkmcnt(0)
	v_mfma_f32_32x32x16_bf16 v[114:129], v[64:67], v[162:165], 0
	v_mfma_f32_32x32x16_bf16 v[80:95], v[64:67], v[178:181], 0
	v_mfma_f32_32x32x16_bf16 v[130:145], v[68:71], v[162:165], 0
	v_mfma_f32_32x32x16_bf16 v[64:79], v[68:71], v[178:181], 0
	v_mfma_f32_32x32x16_bf16 v[114:129], v[96:99], v[166:169], v[114:129]
	v_mfma_f32_32x32x16_bf16 v[80:95], v[96:99], v[182:185], v[80:95]
	v_mfma_f32_32x32x16_bf16 v[130:145], v[100:103], v[166:169], v[130:145]
	v_mfma_f32_32x32x16_bf16 v[64:79], v[100:103], v[182:185], v[64:79]
	v_add_u32_e32 v100, v104, v224
	v_add_u32_e32 v108, v104, v225
	ds_read_b128 v[96:99], v100 offset:32768
	ds_read_b128 v[100:103], v100 offset:40960
	ds_read_b128 v[104:107], v108 offset:32768
	ds_read_b128 v[108:111], v108 offset:40960
	s_waitcnt lgkmcnt(0)
	v_mfma_f32_32x32x16_bf16 v[114:129], v[96:99], v[170:173], v[114:129]
	v_mfma_f32_32x32x16_bf16 v[80:95], v[96:99], v[186:189], v[80:95]
	v_mfma_f32_32x32x16_bf16 v[130:145], v[100:103], v[170:173], v[130:145]
	v_mfma_f32_32x32x16_bf16 v[64:79], v[100:103], v[186:189], v[64:79]
	v_mfma_f32_32x32x16_bf16 v[114:129], v[104:107], v[174:177], v[114:129]
	v_mfma_f32_32x32x16_bf16 v[80:95], v[104:107], v[190:193], v[80:95]
	v_mfma_f32_32x32x16_bf16 v[130:145], v[108:111], v[174:177], v[130:145]
	v_mfma_f32_32x32x16_bf16 v[64:79], v[108:111], v[190:193], v[64:79]
	v_cndmask_b32_e64 v96, 0, 1, s[40:41]
	v_cmp_ne_u32_e64 s[44:45], 1, v96
	s_andn2_b64 vcc, exec, s[40:41]
	s_mov_b64 s[2:3], -1
	s_cbranch_vccnz .LBB0_640
	s_nop 3
	s_setprio 1
	v_exp_f32_e32 v96, v114
	v_exp_f32_e32 v97, v115
	v_exp_f32_e32 v98, v116
	v_exp_f32_e32 v99, v117
	v_exp_f32_e32 v100, v118
	v_exp_f32_e32 v101, v119
	v_exp_f32_e32 v102, v120
	v_exp_f32_e32 v103, v121
	v_exp_f32_e32 v104, v122
	v_exp_f32_e32 v105, v123
	v_exp_f32_e32 v106, v124
	v_exp_f32_e32 v107, v125
	v_exp_f32_e32 v108, v126
	v_exp_f32_e32 v109, v127
	v_exp_f32_e32 v110, v128
	s_setprio 0
	s_cbranch_execz .LBB0_641

.LBB0_644:
	v_exp_f32_e32 v111, v129
	v_exp_f32_e32 v127, v145
	v_cvt_pk_bf16_f32 v194, v96, v97
	v_cvt_pk_bf16_f32 v195, v98, v99
	v_cvt_pk_bf16_f32 v196, v100, v101
	v_cvt_pk_bf16_f32 v197, v102, v103
	v_cvt_pk_bf16_f32 v198, v104, v105
	v_cvt_pk_bf16_f32 v199, v106, v107
	v_cvt_pk_bf16_f32 v200, v108, v109
	v_cvt_pk_bf16_f32 v201, v110, v111
	v_cvt_pk_bf16_f32 v202, v112, v113
	v_cvt_pk_bf16_f32 v203, v114, v115
	v_cvt_pk_bf16_f32 v204, v116, v117
	v_cvt_pk_bf16_f32 v205, v118, v119
	v_cvt_pk_bf16_f32 v206, v120, v121
	v_cvt_pk_bf16_f32 v207, v122, v123
	v_cvt_pk_bf16_f32 v208, v124, v125
	v_cvt_pk_bf16_f32 v209, v126, v127
	v_permlane32_swap_b32_e32 v194, v196
	v_permlane32_swap_b32_e32 v195, v197
	v_permlane32_swap_b32_e32 v198, v200
	v_permlane32_swap_b32_e32 v199, v201
	v_permlane32_swap_b32_e32 v202, v204
	v_permlane32_swap_b32_e32 v203, v205
	v_permlane32_swap_b32_e32 v206, v208
	v_permlane32_swap_b32_e32 v207, v209
	s_and_b64 vcc, exec, s[44:45]
	s_mov_b64 s[2:3], -1
	s_cbranch_vccnz .LBB0_648
	s_setprio 1
	v_exp_f32_e32 v128, v80
	v_exp_f32_e32 v129, v81
	v_exp_f32_e32 v130, v82
	v_exp_f32_e32 v131, v83
	v_exp_f32_e32 v132, v84
	v_exp_f32_e32 v133, v85
	v_exp_f32_e32 v134, v86
	v_exp_f32_e32 v135, v87
	v_exp_f32_e32 v136, v88
	v_exp_f32_e32 v137, v89
	v_exp_f32_e32 v138, v90
	v_exp_f32_e32 v139, v91
	v_exp_f32_e32 v140, v92
	v_exp_f32_e32 v141, v93
	v_exp_f32_e32 v142, v94
	s_setprio 0
	s_cbranch_execz .LBB0_649

.LBB0_663:
	ds_read_b128 v[64:67], v213 offset:32768
	ds_read_b128 v[68:71], v213 offset:40960
	ds_read_b128 v[72:75], v241 offset:32768
	ds_read_b128 v[76:79], v241 offset:40960
	ds_read_b128 v[114:117], v244 offset:32768
	ds_read_b128 v[118:121], v244 offset:40960
	ds_read_b128 v[122:125], v246 offset:32768
	ds_read_b128 v[126:129], v246 offset:40960
	s_waitcnt lgkmcnt(7)
	v_mfma_f32_32x32x16_bf16 v[82:97], v[64:67], v[162:165], 0
	s_waitcnt lgkmcnt(6)
	v_mfma_f32_32x32x16_bf16 v[98:113], v[68:71], v[162:165], 0
	s_waitcnt lgkmcnt(5)
	v_mfma_f32_32x32x16_bf16 v[82:97], v[72:75], v[166:169], v[82:97]
	s_waitcnt lgkmcnt(4)
	v_mfma_f32_32x32x16_bf16 v[98:113], v[76:79], v[166:169], v[98:113]
	s_waitcnt lgkmcnt(3)
	v_mfma_f32_32x32x16_bf16 v[82:97], v[114:117], v[170:173], v[82:97]
	s_waitcnt lgkmcnt(2)
	v_mfma_f32_32x32x16_bf16 v[98:113], v[118:121], v[170:173], v[98:113]
	s_waitcnt lgkmcnt(1)
	v_mfma_f32_32x32x16_bf16 v[82:97], v[122:125], v[174:177], v[82:97]
	s_waitcnt lgkmcnt(0)
	v_mfma_f32_32x32x16_bf16 v[98:113], v[126:129], v[174:177], v[98:113]
	ds_read_b128 v[64:67], v247 offset:32768
	ds_read_b128 v[68:71], v247 offset:40960
	ds_read_b128 v[72:75], v249 offset:32768
	ds_read_b128 v[76:79], v249 offset:40960
	ds_read_b128 v[114:117], v226 offset:32768
	ds_read_b128 v[118:121], v226 offset:40960
	ds_read_b128 v[122:125], v227 offset:32768
	ds_read_b128 v[126:129], v227 offset:40960
	s_waitcnt lgkmcnt(7)
	v_mfma_f32_32x32x16_bf16 v[82:97], v[64:67], v[178:181], v[82:97]
	s_waitcnt lgkmcnt(6)
	v_mfma_f32_32x32x16_bf16 v[98:113], v[68:71], v[178:181], v[98:113]
	s_waitcnt lgkmcnt(5)
	v_mfma_f32_32x32x16_bf16 v[82:97], v[72:75], v[182:185], v[82:97]
	s_waitcnt lgkmcnt(4)
	v_mfma_f32_32x32x16_bf16 v[98:113], v[76:79], v[182:185], v[98:113]
	s_waitcnt lgkmcnt(3)
	v_mfma_f32_32x32x16_bf16 v[82:97], v[114:117], v[186:189], v[82:97]
	s_waitcnt lgkmcnt(2)
	v_mfma_f32_32x32x16_bf16 v[98:113], v[118:121], v[186:189], v[98:113]
	s_waitcnt lgkmcnt(1)
	v_mfma_f32_32x32x16_bf16 v[82:97], v[122:125], v[190:193], v[82:97]
	s_waitcnt lgkmcnt(0)
	v_mfma_f32_32x32x16_bf16 v[98:113], v[126:129], v[190:193], v[98:113]
	s_barrier
	v_cndmask_b32_e64 v64, 0, 1, s[40:41]
	v_cmp_ne_u32_e64 s[42:43], 1, v64
	s_andn2_b64 vcc, exec, s[40:41]
	s_mov_b64 s[2:3], -1
	s_cbranch_vccnz .LBB0_667
	s_nop 3
	s_setprio 1
	v_exp_f32_e32 v64, v82
	v_exp_f32_e32 v65, v83
	v_exp_f32_e32 v66, v84
	v_exp_f32_e32 v67, v85
	v_exp_f32_e32 v68, v86
	v_exp_f32_e32 v69, v87
	v_exp_f32_e32 v70, v88
	v_exp_f32_e32 v71, v89
	v_exp_f32_e32 v72, v90
	v_exp_f32_e32 v73, v91
	v_exp_f32_e32 v74, v92
	v_exp_f32_e32 v75, v93
	v_exp_f32_e32 v76, v94
	v_exp_f32_e32 v77, v95
	v_exp_f32_e32 v78, v96
	s_setprio 0
	s_cbranch_execz .LBB0_668

.LBB0_673:
	ds_read_b64_tr_b16 v[112:113], v231 offset:0
	ds_read_b64_tr_b16 v[114:115], v231 offset:0x800
	ds_read_b64_tr_b16 v[116:117], v231 offset:0x1000
	ds_read_b64_tr_b16 v[118:119], v231 offset:0x1800
	ds_read_b64_tr_b16 v[120:121], v231 offset:0x2000
	ds_read_b64_tr_b16 v[122:123], v231 offset:0x2800
	ds_read_b64_tr_b16 v[124:125], v231 offset:0x3000
	ds_read_b64_tr_b16 v[126:127], v231 offset:0x3800
	s_waitcnt lgkmcnt(0)
	s_nop 0
	v_mfma_f32_32x32x16_bf16 v[0:15], v[96:99], v[112:115], v[0:15]
	ds_read_b64_tr_b16 v[112:113], v231 offset:0x200
	ds_read_b64_tr_b16 v[114:115], v231 offset:0xa00
	v_mfma_f32_32x32x16_bf16 v[0:15], v[100:103], v[116:119], v[0:15]
	ds_read_b64_tr_b16 v[116:117], v231 offset:0x1200
	ds_read_b64_tr_b16 v[118:119], v231 offset:0x1a00
	v_mfma_f32_32x32x16_bf16 v[0:15], v[104:107], v[120:123], v[0:15]
	ds_read_b64_tr_b16 v[120:121], v231 offset:0x2200
	ds_read_b64_tr_b16 v[122:123], v231 offset:0x2a00
	v_mfma_f32_32x32x16_bf16 v[0:15], v[108:111], v[124:127], v[0:15]
	ds_read_b64_tr_b16 v[124:125], v231 offset:0x3200
	ds_read_b64_tr_b16 v[126:127], v231 offset:0x3a00
	s_waitcnt lgkmcnt(0)
	v_mfma_f32_32x32x16_bf16 v[16:31], v[96:99], v[112:115], v[16:31]
	ds_read_b64_tr_b16 v[112:113], v231 offset:0x400
	ds_read_b64_tr_b16 v[114:115], v231 offset:0xc00
	v_mfma_f32_32x32x16_bf16 v[16:31], v[100:103], v[116:119], v[16:31]
	ds_read_b64_tr_b16 v[116:117], v231 offset:0x1400
	ds_read_b64_tr_b16 v[118:119], v231 offset:0x1c00
	v_mfma_f32_32x32x16_bf16 v[16:31], v[104:107], v[120:123], v[16:31]
	ds_read_b64_tr_b16 v[120:121], v231 offset:0x2400
	ds_read_b64_tr_b16 v[122:123], v231 offset:0x2c00
	v_mfma_f32_32x32x16_bf16 v[16:31], v[108:111], v[124:127], v[16:31]
	ds_read_b64_tr_b16 v[124:125], v231 offset:0x3400
	ds_read_b64_tr_b16 v[126:127], v231 offset:0x3c00
	s_waitcnt lgkmcnt(0)
	v_mfma_f32_32x32x16_bf16 v[32:47], v[96:99], v[112:115], v[32:47]
	ds_read_b64_tr_b16 v[112:113], v231 offset:0x600
	ds_read_b64_tr_b16 v[114:115], v231 offset:0xe00
	v_mfma_f32_32x32x16_bf16 v[32:47], v[100:103], v[116:119], v[32:47]
	ds_read_b64_tr_b16 v[116:117], v231 offset:0x1600
	ds_read_b64_tr_b16 v[118:119], v231 offset:0x1e00
	v_mfma_f32_32x32x16_bf16 v[32:47], v[104:107], v[120:123], v[32:47]
	ds_read_b64_tr_b16 v[120:121], v231 offset:0x2600
	ds_read_b64_tr_b16 v[122:123], v231 offset:0x2e00
	v_mfma_f32_32x32x16_bf16 v[32:47], v[108:111], v[124:127], v[32:47]
	ds_read_b64_tr_b16 v[124:125], v231 offset:0x3600
	ds_read_b64_tr_b16 v[126:127], v231 offset:0x3e00
	s_waitcnt lgkmcnt(0)
	v_mfma_f32_32x32x16_bf16 v[48:63], v[96:99], v[112:115], v[48:63]
	v_mfma_f32_32x32x16_bf16 v[48:63], v[100:103], v[116:119], v[48:63]
	v_mfma_f32_32x32x16_bf16 v[48:63], v[104:107], v[120:123], v[48:63]
	v_mfma_f32_32x32x16_bf16 v[48:63], v[108:111], v[124:127], v[48:63]
	ds_read_b128 v[96:99], v213 offset:49152
	ds_read_b128 v[100:103], v213 offset:57344
	ds_read_b128 v[104:107], v241 offset:49152
	ds_read_b128 v[108:111], v241 offset:57344
	ds_read_b128 v[144:147], v244 offset:49152
	ds_read_b128 v[148:151], v244 offset:57344
	ds_read_b128 v[152:155], v246 offset:49152
	ds_read_b128 v[156:159], v246 offset:57344
	s_waitcnt lgkmcnt(7)
	v_mfma_f32_32x32x16_bf16 v[112:127], v[96:99], v[162:165], 0
	s_waitcnt lgkmcnt(6)
	v_mfma_f32_32x32x16_bf16 v[128:143], v[100:103], v[162:165], 0
	s_waitcnt lgkmcnt(5)
	v_mfma_f32_32x32x16_bf16 v[112:127], v[104:107], v[166:169], v[112:127]
	s_waitcnt lgkmcnt(4)
	v_mfma_f32_32x32x16_bf16 v[128:143], v[108:111], v[166:169], v[128:143]
	s_waitcnt lgkmcnt(3)
	v_mfma_f32_32x32x16_bf16 v[112:127], v[144:147], v[170:173], v[112:127]
	s_waitcnt lgkmcnt(2)
	v_mfma_f32_32x32x16_bf16 v[128:143], v[148:151], v[170:173], v[128:143]
	s_waitcnt lgkmcnt(1)
	v_mfma_f32_32x32x16_bf16 v[112:127], v[152:155], v[174:177], v[112:127]
	s_waitcnt lgkmcnt(0)
	v_mfma_f32_32x32x16_bf16 v[128:143], v[156:159], v[174:177], v[128:143]
	ds_read_b128 v[96:99], v247 offset:49152
	ds_read_b128 v[100:103], v247 offset:57344
	ds_read_b128 v[104:107], v249 offset:49152
	ds_read_b128 v[108:111], v249 offset:57344
	ds_read_b128 v[144:147], v226 offset:49152
	ds_read_b128 v[148:151], v226 offset:57344
	ds_read_b128 v[152:155], v227 offset:49152
	ds_read_b128 v[156:159], v227 offset:57344
	s_waitcnt lgkmcnt(7)
	v_mfma_f32_32x32x16_bf16 v[112:127], v[96:99], v[178:181], v[112:127]
	s_waitcnt lgkmcnt(6)
	v_mfma_f32_32x32x16_bf16 v[128:143], v[100:103], v[178:181], v[128:143]
	s_waitcnt lgkmcnt(5)
	v_mfma_f32_32x32x16_bf16 v[112:127], v[104:107], v[182:185], v[112:127]
	s_waitcnt lgkmcnt(4)
	v_mfma_f32_32x32x16_bf16 v[128:143], v[108:111], v[182:185], v[128:143]
	s_waitcnt lgkmcnt(3)
	v_mfma_f32_32x32x16_bf16 v[112:127], v[144:147], v[186:189], v[112:127]
	s_waitcnt lgkmcnt(2)
	v_mfma_f32_32x32x16_bf16 v[128:143], v[148:151], v[186:189], v[128:143]
	s_waitcnt lgkmcnt(1)
	v_mfma_f32_32x32x16_bf16 v[112:127], v[152:155], v[190:193], v[112:127]
	s_waitcnt lgkmcnt(0)
	v_mfma_f32_32x32x16_bf16 v[128:143], v[156:159], v[190:193], v[128:143]
	s_barrier
	s_and_b64 vcc, exec, s[42:43]
	s_mov_b64 s[2:3], -1
	s_cbranch_vccnz .LBB0_677
	s_nop 5
	s_setprio 1
	v_exp_f32_e32 v96, v112
	v_exp_f32_e32 v97, v113
	v_exp_f32_e32 v98, v114
	v_exp_f32_e32 v99, v115
	v_exp_f32_e32 v100, v116
	v_exp_f32_e32 v101, v117
	v_exp_f32_e32 v102, v118
	v_exp_f32_e32 v103, v119
	v_exp_f32_e32 v104, v120
	v_exp_f32_e32 v105, v121
	v_exp_f32_e32 v106, v122
	v_exp_f32_e32 v107, v123
	v_exp_f32_e32 v108, v124
	v_exp_f32_e32 v109, v125
	v_exp_f32_e32 v110, v126
	s_setprio 0
	s_cbranch_execz .LBB0_678

.LBB0_687:
	s_lshl_b64 s[2:3], s[2:3], 1
	s_add_u32 s2, s18, s2
	s_addc_u32 s3, s19, s3
	global_load_dwordx4 v[146:149], v210, s[2:3]
	global_load_dwordx4 v[150:153], v210, s[2:3] offset:256
	global_load_dwordx4 v[154:157], v212, s[2:3]
	global_load_dwordx4 v[194:197], v212, s[2:3] offset:256
	ds_read_b128 v[64:67], v204 offset:32768
	ds_read_b128 v[68:71], v204 offset:40960
	ds_read_b128 v[72:75], v205 offset:32768
	ds_read_b128 v[76:79], v205 offset:40960
	ds_read_b128 v[80:83], v206 offset:32768
	ds_read_b128 v[84:87], v206 offset:40960
	ds_read_b128 v[88:91], v207 offset:32768
	ds_read_b128 v[92:95], v207 offset:40960
	s_waitcnt lgkmcnt(7)
	v_mfma_f32_32x32x16_bf16 v[112:127], v[64:67], v[162:165], 0
	s_waitcnt lgkmcnt(6)
	v_mfma_f32_32x32x16_bf16 v[96:111], v[68:71], v[162:165], 0
	s_waitcnt lgkmcnt(5)
	v_mfma_f32_32x32x16_bf16 v[112:127], v[72:75], v[166:169], v[112:127]
	s_waitcnt lgkmcnt(4)
	v_mfma_f32_32x32x16_bf16 v[96:111], v[76:79], v[166:169], v[96:111]
	s_waitcnt lgkmcnt(3)
	v_mfma_f32_32x32x16_bf16 v[112:127], v[80:83], v[170:173], v[112:127]
	s_waitcnt lgkmcnt(2)
	v_mfma_f32_32x32x16_bf16 v[96:111], v[84:87], v[170:173], v[96:111]
	s_waitcnt lgkmcnt(1)
	v_mfma_f32_32x32x16_bf16 v[112:127], v[88:91], v[174:177], v[112:127]
	s_waitcnt lgkmcnt(0)
	v_mfma_f32_32x32x16_bf16 v[96:111], v[92:95], v[174:177], v[96:111]
	ds_read_b128 v[64:67], v208 offset:32768
	ds_read_b128 v[68:71], v208 offset:40960
	ds_read_b128 v[72:75], v209 offset:32768
	ds_read_b128 v[76:79], v209 offset:40960
	ds_read_b128 v[80:83], v213 offset:32768
	ds_read_b128 v[84:87], v213 offset:40960
	ds_read_b128 v[88:91], v214 offset:32768
	ds_read_b128 v[92:95], v214 offset:40960
	s_waitcnt lgkmcnt(7)
	v_mfma_f32_32x32x16_bf16 v[112:127], v[64:67], v[178:181], v[112:127]
	s_waitcnt lgkmcnt(6)
	v_mfma_f32_32x32x16_bf16 v[96:111], v[68:71], v[178:181], v[96:111]
	s_waitcnt lgkmcnt(5)
	v_mfma_f32_32x32x16_bf16 v[112:127], v[72:75], v[182:185], v[112:127]
	s_waitcnt lgkmcnt(4)
	v_mfma_f32_32x32x16_bf16 v[96:111], v[76:79], v[182:185], v[96:111]
	s_waitcnt lgkmcnt(3)
	v_mfma_f32_32x32x16_bf16 v[112:127], v[80:83], v[186:189], v[112:127]
	s_waitcnt lgkmcnt(2)
	v_mfma_f32_32x32x16_bf16 v[96:111], v[84:87], v[186:189], v[96:111]
	s_waitcnt lgkmcnt(1)
	v_mfma_f32_32x32x16_bf16 v[112:127], v[88:91], v[190:193], v[112:127]
	s_waitcnt lgkmcnt(0)
	v_mfma_f32_32x32x16_bf16 v[96:111], v[92:95], v[190:193], v[96:111]
	v_cndmask_b32_e64 v64, 0, 1, s[40:41]
	v_cmp_ne_u32_e64 s[42:43], 1, v64
	s_andn2_b64 vcc, exec, s[40:41]
	s_mov_b64 s[2:3], -1
	s_cbranch_vccnz .LBB0_691
	s_nop 4
	s_setprio 1
	v_exp_f32_e32 v64, v112
	v_exp_f32_e32 v65, v113
	v_exp_f32_e32 v66, v114
	v_exp_f32_e32 v67, v115
	v_exp_f32_e32 v68, v116
	v_exp_f32_e32 v69, v117
	v_exp_f32_e32 v70, v118
	v_exp_f32_e32 v71, v119
	v_exp_f32_e32 v72, v120
	v_exp_f32_e32 v73, v121
	v_exp_f32_e32 v74, v122
	v_exp_f32_e32 v75, v123
	v_exp_f32_e32 v76, v124
	v_exp_f32_e32 v77, v125
	v_exp_f32_e32 v78, v126
	s_setprio 0
	s_cbranch_execz .LBB0_692

.LBB0_697:
	ds_read_b128 v[96:99], v204 offset:49152
	ds_read_b128 v[100:103], v204 offset:57344
	ds_read_b128 v[104:107], v205 offset:49152
	ds_read_b128 v[108:111], v205 offset:57344
	ds_read_b128 v[216:219], v206 offset:49152
	ds_read_b128 v[226:229], v206 offset:57344
	ds_read_b128 v[236:239], v207 offset:49152
	ds_read_b128 v[246:249], v207 offset:57344
	s_waitcnt lgkmcnt(7)
	v_mfma_f32_32x32x16_bf16 v[114:129], v[96:99], v[162:165], 0
	s_waitcnt lgkmcnt(6)
	v_mfma_f32_32x32x16_bf16 v[130:145], v[100:103], v[162:165], 0
	s_waitcnt lgkmcnt(5)
	v_mfma_f32_32x32x16_bf16 v[114:129], v[104:107], v[166:169], v[114:129]
	s_waitcnt lgkmcnt(4)
	v_mfma_f32_32x32x16_bf16 v[130:145], v[108:111], v[166:169], v[130:145]
	s_waitcnt lgkmcnt(3)
	v_mfma_f32_32x32x16_bf16 v[114:129], v[216:219], v[170:173], v[114:129]
	s_waitcnt lgkmcnt(2)
	v_mfma_f32_32x32x16_bf16 v[130:145], v[226:229], v[170:173], v[130:145]
	s_waitcnt lgkmcnt(1)
	v_mfma_f32_32x32x16_bf16 v[114:129], v[236:239], v[174:177], v[114:129]
	s_waitcnt lgkmcnt(0)
	v_mfma_f32_32x32x16_bf16 v[130:145], v[246:249], v[174:177], v[130:145]
	ds_read_b128 v[96:99], v208 offset:49152
	ds_read_b128 v[100:103], v208 offset:57344
	ds_read_b128 v[104:107], v209 offset:49152
	ds_read_b128 v[108:111], v209 offset:57344
	ds_read_b128 v[216:219], v213 offset:49152
	ds_read_b128 v[226:229], v213 offset:57344
	ds_read_b128 v[236:239], v214 offset:49152
	ds_read_b128 v[246:249], v214 offset:57344
	s_waitcnt lgkmcnt(7)
	v_mfma_f32_32x32x16_bf16 v[114:129], v[96:99], v[178:181], v[114:129]
	s_waitcnt lgkmcnt(6)
	v_mfma_f32_32x32x16_bf16 v[130:145], v[100:103], v[178:181], v[130:145]
	s_waitcnt lgkmcnt(5)
	v_mfma_f32_32x32x16_bf16 v[114:129], v[104:107], v[182:185], v[114:129]
	s_waitcnt lgkmcnt(4)
	v_mfma_f32_32x32x16_bf16 v[130:145], v[108:111], v[182:185], v[130:145]
	s_waitcnt lgkmcnt(3)
	v_mfma_f32_32x32x16_bf16 v[114:129], v[216:219], v[186:189], v[114:129]
	s_waitcnt lgkmcnt(2)
	v_mfma_f32_32x32x16_bf16 v[130:145], v[226:229], v[186:189], v[130:145]
	s_waitcnt lgkmcnt(1)
	v_mfma_f32_32x32x16_bf16 v[114:129], v[236:239], v[190:193], v[114:129]
	s_waitcnt lgkmcnt(0)
	v_mfma_f32_32x32x16_bf16 v[130:145], v[246:249], v[190:193], v[130:145]
	s_and_b64 vcc, exec, s[42:43]
	s_mov_b64 s[2:3], -1
	s_cbranch_vccnz .LBB0_701
	s_nop 6
	s_setprio 1
	v_exp_f32_e32 v96, v114
	v_exp_f32_e32 v97, v115
	v_exp_f32_e32 v98, v116
	v_exp_f32_e32 v99, v117
	v_exp_f32_e32 v100, v118
	v_exp_f32_e32 v101, v119
	v_exp_f32_e32 v102, v120
	v_exp_f32_e32 v103, v121
	v_exp_f32_e32 v104, v122
	v_exp_f32_e32 v105, v123
	v_exp_f32_e32 v106, v124
	v_exp_f32_e32 v107, v125
	v_exp_f32_e32 v108, v126
	v_exp_f32_e32 v109, v127
	v_exp_f32_e32 v110, v128
	s_setprio 0
	s_cbranch_execz .LBB0_702
